# speedup vs baseline: 1.0084x; 1.0084x over previous
.LBB1_11:
	s_lshl_b32 s0, s30, 5
	s_lshl_b32 s1, s31, 7
	s_and_b32 s13, s2, 3
	s_or_b32 s14, s0, s1
	s_lshl_b32 s4, s28, 7
	s_lshl_b32 s5, s31, 2
	s_add_i32 s4, s4, s5
	s_add_i32 s4, s4, s30
	s_lshl_b32 s4, s4, 1
	s_add_i32 s4, s4, s3
	s_lshl_b32 s4, s4, 12
	s_add_u32 s4, s18, s4
	s_addc_u32 s5, s19, 0
	v_lshlrev_b32_e32 v0, 2, v173
	s_lshl_b32 s0, s3, 5
	s_lshl_b32 s12, s13, 6
	s_mov_b32 s1, 0
	s_mov_b32 s15, 0
	global_load_dwordx4 v[124:127], v0, s[4:5]
	global_load_dwordx4 v[128:131], v0, s[4:5] offset:1024
	global_load_dwordx4 v[132:135], v0, s[4:5] offset:2048
	global_load_dwordx4 v[136:139], v0, s[4:5] offset:3072
	s_lshl_b64 s[2:3], s[14:15], 2
	v_mov_b32_e32 v37, 0
	v_lshlrev_b32_e32 v36, 2, v172
	v_lshlrev_b32_e32 v122, 16, v175
	v_mov_b32_e32 v123, 0
	s_mul_i32 s4, s29, 0x2200
	s_add_i32 s4, s4, 0
	v_mov_b32_e32 v8, v141
	v_add_u32_e32 v9, s4, v173
	s_xor_b32 s4, s29, 4
	v_permlane32_swap_b32_e32 v141, v8
	s_mulk_i32 s4, 0x2200
	v_add_f32_e32 v8, v141, v8
	s_add_i32 s4, s4, 0
	ds_write2st64_b32 v9, v146, v8 offset1:1
	ds_write2st64_b32 v9, v54, v55 offset0:2 offset1:3
	ds_write2st64_b32 v9, v38, v39 offset0:18 offset1:19
	ds_write2st64_b32 v9, v56, v57 offset0:4 offset1:5
	ds_write2st64_b32 v9, v40, v41 offset0:20 offset1:21
	ds_write2st64_b32 v9, v58, v59 offset0:6 offset1:7
	ds_write2st64_b32 v9, v42, v43 offset0:22 offset1:23
	ds_write2st64_b32 v9, v60, v61 offset0:8 offset1:9
	ds_write2st64_b32 v9, v44, v45 offset0:24 offset1:25
	ds_write2st64_b32 v9, v62, v63 offset0:10 offset1:11
	ds_write2st64_b32 v9, v46, v47 offset0:26 offset1:27
	ds_write2st64_b32 v9, v64, v65 offset0:12 offset1:13
	ds_write2st64_b32 v9, v48, v49 offset0:28 offset1:29
	ds_write2st64_b32 v9, v66, v67 offset0:14 offset1:15
	ds_write2st64_b32 v9, v50, v51 offset0:30 offset1:31
	ds_write2st64_b32 v9, v68, v69 offset0:16 offset1:17
	ds_write2st64_b32 v9, v52, v53 offset0:32 offset1:33
	v_add_u32_e32 v66, s4, v173
	s_waitcnt lgkmcnt(0)
	s_barrier
	ds_read2st64_b32 v[10:11], v66 offset1:1
	ds_read2st64_b32 v[12:13], v66 offset0:2 offset1:3
	ds_read2st64_b32 v[14:15], v66 offset0:4 offset1:5
	ds_read2st64_b32 v[38:39], v66 offset0:6 offset1:7
	v_max_f32_e32 v40, v146, v146
	s_waitcnt lgkmcnt(3)
	v_max_f32_e32 v9, v10, v10
	v_max_f32_e32 v9, v40, v9
	v_sub_f32_e32 v40, v146, v9
	v_sub_f32_e32 v9, v10, v9
	v_exp_f32_e32 v40, v40
	v_exp_f32_e32 v41, v9
	v_mov_b32_e32 v9, v11
	v_pk_mul_f32 v[8:9], v[8:9], v[40:41]
	s_nop 0
	v_add_f32_e32 v8, v8, v9
	v_div_scale_f32 v9, s[4:5], v8, v8, 1.0
	v_rcp_f32_e32 v10, v9
	s_nop 0
	v_fma_f32 v11, -v9, v10, 1.0
	v_fmac_f32_e32 v10, v11, v10
	v_div_scale_f32 v11, vcc, 1.0, v8, 1.0
	v_mul_f32_e32 v42, v11, v10
	v_fma_f32 v43, -v9, v42, v11
	v_fmac_f32_e32 v42, v43, v10
	v_fma_f32 v9, -v9, v42, v11
	v_div_fmas_f32 v9, v9, v10, v42
	v_div_fixup_f32 v9, v9, v8, 1.0
	v_mul_f32_e32 v8, v40, v9
	v_mul_f32_e32 v10, v41, v9
	ds_read2st64_b32 v[40:41], v66 offset0:18 offset1:19
	ds_read2st64_b32 v[42:43], v66 offset0:20 offset1:21
	ds_read2st64_b32 v[44:45], v66 offset0:22 offset1:23
	ds_read2st64_b32 v[46:47], v66 offset0:16 offset1:17
	s_waitcnt lgkmcnt(6)
	v_pk_mul_f32 v[12:13], v[10:11], v[12:13] op_sel_hi:[0,1]
	s_waitcnt lgkmcnt(5)
	v_pk_mul_f32 v[14:15], v[10:11], v[14:15] op_sel_hi:[0,1]
	s_waitcnt lgkmcnt(4)
	v_pk_mul_f32 v[38:39], v[10:11], v[38:39] op_sel_hi:[0,1]
	s_waitcnt lgkmcnt(3)
	v_pk_mul_f32 v[40:41], v[10:11], v[40:41] op_sel_hi:[0,1]
	v_pk_fma_f32 v[48:49], v[8:9], v[70:71], v[40:41] op_sel_hi:[0,1,1]
	s_waitcnt lgkmcnt(2)
	v_pk_mul_f32 v[40:41], v[10:11], v[42:43] op_sel_hi:[0,1]
	v_pk_fma_f32 v[50:51], v[8:9], v[72:73], v[40:41] op_sel_hi:[0,1,1]
	s_waitcnt lgkmcnt(1)
	v_pk_mul_f32 v[40:41], v[10:11], v[44:45] op_sel_hi:[0,1]
	v_pk_fma_f32 v[52:53], v[8:9], v[74:75], v[40:41] op_sel_hi:[0,1,1]
	ds_read2st64_b32 v[40:41], v66 offset0:8 offset1:9
	ds_read2st64_b32 v[42:43], v66 offset0:24 offset1:25
	ds_read2st64_b32 v[44:45], v66 offset0:10 offset1:11
	ds_read2st64_b32 v[54:55], v66 offset0:12 offset1:13
	ds_read2st64_b32 v[56:57], v66 offset0:14 offset1:15
	ds_read2st64_b32 v[58:59], v66 offset0:26 offset1:27
	ds_read2st64_b32 v[60:61], v66 offset0:28 offset1:29
	ds_read2st64_b32 v[62:63], v66 offset0:30 offset1:31
	s_waitcnt lgkmcnt(6)
	v_pk_mul_f32 v[42:43], v[10:11], v[42:43] op_sel_hi:[0,1]
	v_pk_fma_f32 v[64:65], v[8:9], v[76:77], v[42:43] op_sel_hi:[0,1,1]
	s_waitcnt lgkmcnt(5)
	v_pk_mul_f32 v[42:43], v[10:11], v[44:45] op_sel_hi:[0,1]
	s_waitcnt lgkmcnt(2)
	v_pk_mul_f32 v[44:45], v[10:11], v[58:59] op_sel_hi:[0,1]
	v_pk_fma_f32 v[58:59], v[8:9], v[78:79], v[44:45] op_sel_hi:[0,1,1]
	v_pk_mul_f32 v[44:45], v[10:11], v[54:55] op_sel_hi:[0,1]
	s_waitcnt lgkmcnt(1)
	v_pk_mul_f32 v[54:55], v[10:11], v[60:61] op_sel_hi:[0,1]
	ds_read2st64_b32 v[60:61], v66 offset0:32 offset1:33
	s_waitcnt vmcnt(0)
	v_pk_mul_f32 v[40:41], v[10:11], v[40:41] op_sel_hi:[0,1]
	v_cvt_pk_bf16_f32 v0, v208, v209
	v_cvt_pk_bf16_f32 v1, v210, v211
	v_cvt_pk_bf16_f32 v2, v212, v213
	v_cvt_pk_bf16_f32 v3, v214, v215
	v_pk_fma_f32 v[12:13], v[8:9], v[86:87], v[12:13] op_sel_hi:[0,1,1]
	v_pk_fma_f32 v[14:15], v[8:9], v[88:89], v[14:15] op_sel_hi:[0,1,1]
	v_pk_fma_f32 v[38:39], v[8:9], v[90:91], v[38:39] op_sel_hi:[0,1,1]
	v_pk_fma_f32 v[40:41], v[8:9], v[92:93], v[40:41] op_sel_hi:[0,1,1]
	v_pk_mul_f32 v[56:57], v[10:11], v[56:57] op_sel_hi:[0,1]
	s_waitcnt lgkmcnt(1)
	v_pk_mul_f32 v[62:63], v[10:11], v[62:63] op_sel_hi:[0,1]
	v_pk_mul_f32 v[46:47], v[10:11], v[46:47] op_sel_hi:[0,1]
	s_waitcnt lgkmcnt(0)
	v_pk_mul_f32 v[10:11], v[10:11], v[60:61] op_sel_hi:[0,1]
	v_cvt_pk_bf16_f32 v4, v12, v13
	v_cvt_pk_bf16_f32 v5, v14, v15
	v_cvt_pk_bf16_f32 v6, v38, v39
	v_cvt_pk_bf16_f32 v7, v40, v41
	v_pk_fma_f32 v[42:43], v[8:9], v[94:95], v[42:43] op_sel_hi:[0,1,1]
	v_pk_fma_f32 v[44:45], v[8:9], v[96:97], v[44:45] op_sel_hi:[0,1,1]
	v_pk_fma_f32 v[54:55], v[8:9], v[80:81], v[54:55] op_sel_hi:[0,1,1]
	v_pk_fma_f32 v[56:57], v[8:9], v[98:99], v[56:57] op_sel_hi:[0,1,1]
	v_pk_fma_f32 v[62:63], v[8:9], v[82:83], v[62:63] op_sel_hi:[0,1,1]
	v_pk_fma_f32 v[46:47], v[8:9], v[100:101], v[46:47] op_sel_hi:[0,1,1]
	v_pk_fma_f32 v[60:61], v[8:9], v[84:85], v[10:11] op_sel_hi:[0,1,1]
	v_mfma_f32_32x32x16_bf16 v[0:15], v[0:3], v[4:7], 0
	v_cvt_pk_bf16_f32 v42, v42, v43
	v_cvt_pk_bf16_f32 v38, v216, v217
	v_cvt_pk_bf16_f32 v39, v218, v219
	v_cvt_pk_bf16_f32 v40, v220, v221
	v_cvt_pk_bf16_f32 v41, v222, v223
	v_cvt_pk_bf16_f32 v43, v44, v45
	v_cvt_pk_bf16_f32 v44, v56, v57
	v_cvt_pk_bf16_f32 v45, v46, v47
	s_nop 1
	v_mfma_f32_32x32x16_bf16 v[0:15], v[38:41], v[42:45], v[0:15]
	v_cvt_pk_bf16_f32 v38, v224, v225
	v_cvt_pk_bf16_f32 v39, v226, v227
	v_cvt_pk_bf16_f32 v40, v228, v229
	v_cvt_pk_bf16_f32 v41, v230, v231
	v_cvt_pk_bf16_f32 v42, v48, v49
	v_cvt_pk_bf16_f32 v43, v50, v51
	v_cvt_pk_bf16_f32 v44, v52, v53
	v_cvt_pk_bf16_f32 v45, v64, v65
	v_cvt_pk_bf16_f32 v32, v232, v233
	v_cvt_pk_bf16_f32 v33, v234, v235
	v_mfma_f32_32x32x16_bf16 v[0:15], v[38:41], v[42:45], v[0:15]
	v_cvt_pk_bf16_f32 v34, v236, v237
	v_cvt_pk_bf16_f32 v35, v238, v239
	v_cvt_pk_bf16_f32 v38, v58, v59
	v_add_f32_e32 v42, 1.0, v205
	v_div_scale_f32 v43, s[4:5], v42, v42, 1.0
	v_rcp_f32_e32 v44, v43
	v_cvt_pk_bf16_f32 v39, v54, v55
	v_cvt_pk_bf16_f32 v40, v62, v63
	v_cvt_pk_bf16_f32 v41, v60, v61
	s_lshl_b32 s4, s28, 8
	s_or_b32 s4, s4, s12
	v_mfma_f32_32x32x16_bf16 v[0:15], v[32:35], v[38:41], v[0:15]
	v_fma_f32 v32, -v43, v44, 1.0
	v_fmac_f32_e32 v44, v32, v44
	v_div_scale_f32 v32, vcc, 1.0, v42, 1.0
	s_add_i32 s0, s4, s0
	v_mul_f32_e32 v33, v32, v44
	s_lshl_b64 s[0:1], s[0:1], 14
	v_fma_f32 v34, -v43, v33, v32
	s_add_u32 s0, s10, s0
	v_fmac_f32_e32 v33, v34, v44
	s_addc_u32 s1, s11, s1
	v_fma_f32 v32, -v43, v33, v32
	s_add_u32 s0, s0, s2
	v_div_fmas_f32 v32, v32, v44, v33
	s_addc_u32 s1, s1, s3
	v_add_f32_e32 v0, v0, v240
	v_div_fixup_f32 v34, v32, v42, 1.0
	v_add_u32_e32 v32, v36, v122
	v_fmac_f32_e32 v124, v205, v0
	v_mul_f32_e32 v0, v34, v124
	global_store_dword v32, v0, s[0:1] sc1
	v_add_f32_e32 v0, v1, v241
	v_fmac_f32_e32 v125, v205, v0
	v_add_u32_e32 v0, 0x4000, v32
	v_mul_f32_e32 v28, v34, v125
	global_store_dword v0, v28, s[0:1] sc1
	v_add_f32_e32 v0, v2, v242
	v_fmac_f32_e32 v126, v205, v0
	v_add_u32_e32 v0, 0x8000, v32
	v_mul_f32_e32 v2, v34, v126
	global_store_dword v0, v2, s[0:1] sc1
	v_add_f32_e32 v0, v3, v243
	v_fmac_f32_e32 v127, v205, v0
	v_add_u32_e32 v0, 0xc000, v32
	v_mul_f32_e32 v2, v34, v127
	global_store_dword v0, v2, s[0:1] sc1
	v_add_f32_e32 v0, v4, v244
	v_fmac_f32_e32 v128, v205, v0
	v_add_u32_e32 v0, 0x20000, v32
	v_mul_f32_e32 v2, v34, v128
	global_store_dword v0, v2, s[0:1] sc1
	v_add_f32_e32 v0, v5, v245
	v_fmac_f32_e32 v129, v205, v0
	v_add_u32_e32 v0, 0x24000, v32
	v_mul_f32_e32 v2, v34, v129
	global_store_dword v0, v2, s[0:1] sc1
	v_add_f32_e32 v0, v6, v246
	v_fmac_f32_e32 v130, v205, v0
	v_add_u32_e32 v0, 0x28000, v32
	v_mul_f32_e32 v2, v34, v130
	global_store_dword v0, v2, s[0:1] sc1
	v_add_f32_e32 v0, v7, v247
	v_fmac_f32_e32 v131, v205, v0
	v_add_u32_e32 v0, 0x2c000, v32
	v_mul_f32_e32 v2, v34, v131
	global_store_dword v0, v2, s[0:1] sc1
	v_add_f32_e32 v0, v8, v248
	v_fmac_f32_e32 v132, v205, v0
	v_add_u32_e32 v0, 0x40000, v32
	v_mul_f32_e32 v2, v34, v132
	global_store_dword v0, v2, s[0:1] sc1
	v_add_f32_e32 v0, v9, v249
	v_fmac_f32_e32 v133, v205, v0
	v_add_u32_e32 v0, 0x44000, v32
	v_mul_f32_e32 v2, v34, v133
	global_store_dword v0, v2, s[0:1] sc1
	v_add_f32_e32 v0, v10, v250
	v_fmac_f32_e32 v134, v205, v0
	v_add_u32_e32 v0, 0x48000, v32
	v_mul_f32_e32 v2, v34, v134
	global_store_dword v0, v2, s[0:1] sc1
	v_add_f32_e32 v0, v11, v251
	v_fmac_f32_e32 v135, v205, v0
	v_add_u32_e32 v0, 0x4c000, v32
	v_mul_f32_e32 v2, v34, v135
	global_store_dword v0, v2, s[0:1] sc1
	v_add_f32_e32 v0, v12, v252
	v_fmac_f32_e32 v136, v205, v0
	v_add_u32_e32 v0, 0x60000, v32
	v_mul_f32_e32 v2, v34, v136
	global_store_dword v0, v2, s[0:1] sc1
	v_add_f32_e32 v0, v13, v253
	v_fmac_f32_e32 v137, v205, v0
	v_add_u32_e32 v0, 0x64000, v32
	v_mul_f32_e32 v2, v34, v137
	global_store_dword v0, v2, s[0:1] sc1
	v_add_f32_e32 v0, v14, v254
	v_fmac_f32_e32 v138, v205, v0
	v_add_u32_e32 v0, 0x68000, v32
	v_mul_f32_e32 v2, v34, v138
	global_store_dword v0, v2, s[0:1] sc1
	v_add_f32_e32 v0, v15, v255
	v_fmac_f32_e32 v139, v205, v0
	v_add_u32_e32 v0, 0x6c000, v32
	v_mul_f32_e32 v2, v34, v139
	global_store_dword v0, v2, s[0:1] sc1
	s_endpgm
